# speedup vs baseline: 1.0351x; 1.0027x over previous
.LBB1_54:
	v_readfirstlane_b32 s23, v0
	s_lshr_b32 s24, s23, 8
	s_lshl_b32 s2, s24, 13
	s_add_i32 s2, s2, 0
	v_add_u32_e32 v199, s2, v211
	v_add_u32_e32 v0, s30, v199
	s_waitcnt lgkmcnt(0)
	v_add_u32_e32 v6, v0, v207
	ds_read_b128 v[2:5], v6
	ds_read_b128 v[6:9], v6 offset:4096
	v_add_u32_e32 v10, v0, v206
	s_waitcnt lgkmcnt(1)
	v_mfma_f32_32x32x16_f16 v[32:47], v[2:5], v[124:127], 0
	s_waitcnt lgkmcnt(0)
	v_mfma_f32_32x32x16_f16 v[16:31], v[6:9], v[124:127], 0
	ds_read_b128 v[2:5], v10
	ds_read_b128 v[6:9], v10 offset:4096
	v_add_u32_e32 v10, v0, v205
	v_add_u32_e32 v0, v0, v204
	s_waitcnt lgkmcnt(1)
	v_mfma_f32_32x32x16_f16 v[32:47], v[2:5], v[120:123], v[32:47]
	s_waitcnt lgkmcnt(0)
	v_mfma_f32_32x32x16_f16 v[16:31], v[6:9], v[120:123], v[16:31]
	ds_read_b128 v[2:5], v10
	ds_read_b128 v[6:9], v10 offset:4096
	s_waitcnt lgkmcnt(1)
	v_mfma_f32_32x32x16_f16 v[32:47], v[2:5], v[116:119], v[32:47]
	ds_read_b128 v[2:5], v0 offset:4096
	s_waitcnt lgkmcnt(1)
	v_mfma_f32_32x32x16_f16 v[16:31], v[6:9], v[116:119], v[16:31]
	s_waitcnt lgkmcnt(0)
	v_mfma_f32_32x32x16_f16 v[16:31], v[2:5], v[112:115], v[16:31]
	ds_read_b128 v[2:5], v0
	s_waitcnt lgkmcnt(0)
	v_mfma_f32_32x32x16_f16 v[32:47], v[2:5], v[112:115], v[32:47]
	s_nop 8
	v_max_f32_e64 v0, |v16|, |v16|
	s_nop 1
	v_max_f32_e64 v2, |v32|, |v32|
	v_min_f32_e32 v0, v2, v0
	v_min3_f32 v0, v0, |v33|, |v17|
	v_min3_f32 v0, v0, |v34|, |v18|
	v_min3_f32 v0, v0, |v35|, |v19|
	v_min3_f32 v0, v0, |v36|, |v20|
	v_min3_f32 v0, v0, |v37|, |v21|
	v_min3_f32 v0, v0, |v38|, |v22|
	v_min3_f32 v0, v0, |v39|, |v23|
	v_min3_f32 v0, v0, |v40|, |v24|
	v_min3_f32 v0, v0, |v41|, |v25|
	v_min3_f32 v0, v0, |v42|, |v26|
	v_min3_f32 v0, v0, |v43|, |v27|
	v_min3_f32 v0, v0, |v44|, |v28|
	v_min3_f32 v0, v0, |v45|, |v29|
	v_min3_f32 v0, v0, |v46|, |v30|
	v_min3_f32 v0, v0, |v47|, |v31|
	v_cmp_eq_f32_e32 vcc, 0, v0
	s_cbranch_vccnz .LBB1_119

.LBB1_57:
	v_add_u32_e32 v0, s2, v191
	v_add3_u32 v197, v0, v209, v210
	v_max_f32_e32 v0, v33, v33
	v_max_f32_e32 v2, v32, v32
	v_max_f32_e32 v0, v2, v0
	v_max3_f32 v2, v34, v35, v17
	v_max3_f32 v0, v0, v16, v18
	v_max3_f32 v0, v0, v19, v36
	v_max3_f32 v2, v2, v38, v39
	v_max3_f32 v0, v0, v37, v20
	v_max3_f32 v2, v2, v22, v23
	v_max3_f32 v0, v0, v21, v40
	v_max3_f32 v2, v2, v42, v43
	v_max3_f32 v0, v0, v41, v24
	v_max3_f32 v2, v2, v26, v27
	v_max3_f32 v0, v0, v25, v44
	v_max3_f32 v2, v2, v46, v47
	v_max3_f32 v0, v0, v45, v28
	v_max3_f32 v2, v2, v30, v31
	v_max3_f32 v0, v0, v29, v2
	v_mov_b32_e32 v2, v0
	s_and_b32 s3, s23, 0x3fffffc0
	s_nop 0
	v_permlane32_swap_b32_e32 v0, v2
	s_lshl_b32 s2, s3, 2
	v_max_f32_e32 v2, v2, v2
	v_max_f32_e32 v0, v0, v0
	s_add_i32 s27, s2, 0
	v_max_f32_e32 v0, v0, v2
	s_mov_b32 s2, 0x41000000
	v_cmp_le_f32_e32 vcc, -4.0, v0
	v_cmp_ge_f32_e64 s[2:3], s2, v0
	v_max_f32_e32 v0, 0xf149f2ca, v0
	s_and_b64 s[2:3], vcc, s[2:3]
	v_cndmask_b32_e64 v192, v0, 0, s[2:3]
	v_add_f32_e64 v0, v32, -v192
	v_exp_f32_e32 v64, v0
	v_add_f32_e64 v0, v16, -v192
	v_exp_f32_e32 v32, v0
	v_add_f32_e64 v0, v33, -v192
	v_exp_f32_e32 v65, v0
	v_add_f32_e64 v0, v17, -v192
	v_exp_f32_e32 v33, v0
	v_add_f32_e64 v0, v34, -v192
	v_exp_f32_e32 v66, v0
	v_add_f32_e64 v0, v18, -v192
	v_exp_f32_e32 v34, v0
	v_add_f32_e64 v0, v35, -v192
	v_exp_f32_e32 v67, v0
	v_add_f32_e64 v0, v19, -v192
	v_exp_f32_e32 v35, v0
	v_add_f32_e64 v0, v36, -v192
	v_exp_f32_e32 v68, v0
	v_add_f32_e64 v0, v20, -v192
	v_exp_f32_e32 v36, v0
	v_add_f32_e64 v0, v37, -v192
	v_exp_f32_e32 v69, v0
	v_add_f32_e64 v0, v21, -v192
	v_exp_f32_e32 v37, v0
	v_add_f32_e64 v0, v38, -v192
	v_exp_f32_e32 v70, v0
	v_add_f32_e64 v0, v22, -v192
	v_exp_f32_e32 v38, v0
	v_add_f32_e64 v0, v39, -v192
	v_exp_f32_e32 v71, v0
	v_add_f32_e64 v0, v23, -v192
	v_exp_f32_e32 v39, v0
	v_add_f32_e64 v0, v40, -v192
	v_exp_f32_e32 v72, v0
	v_add_f32_e64 v0, v24, -v192
	v_exp_f32_e32 v40, v0
	v_add_f32_e64 v0, v41, -v192
	v_exp_f32_e32 v73, v0
	v_add_f32_e64 v0, v25, -v192
	v_exp_f32_e32 v41, v0
	v_add_f32_e64 v0, v42, -v192
	v_exp_f32_e32 v74, v0
	v_add_f32_e64 v0, v26, -v192
	v_exp_f32_e32 v42, v0
	v_add_f32_e64 v0, v43, -v192
	v_exp_f32_e32 v75, v0
	v_add_f32_e64 v0, v27, -v192
	v_exp_f32_e32 v43, v0
	v_add_f32_e64 v0, v44, -v192
	v_exp_f32_e32 v76, v0
	v_add_f32_e64 v0, v28, -v192
	v_exp_f32_e32 v44, v0
	v_add_f32_e64 v0, v45, -v192
	v_exp_f32_e32 v77, v0
	v_add_f32_e64 v0, v29, -v192
	v_exp_f32_e32 v45, v0
	v_add_f32_e64 v0, v46, -v192
	v_exp_f32_e32 v78, v0
	v_add_f32_e64 v0, v30, -v192
	v_exp_f32_e32 v46, v0
	v_add_f32_e64 v0, v47, -v192
	v_exp_f32_e32 v79, v0
	v_add_f32_e64 v0, v31, -v192
	v_exp_f32_e32 v47, v0
	s_bitcmp1_b32 s36, 8
	s_cbranch_scc1 .Lu2w_g1
	s_waitcnt vmcnt(4) lgkmcnt(0)
	s_branch .Lu2w_done
.Lu2w_g1:
	s_waitcnt vmcnt(0) lgkmcnt(0)
.Lu2w_done:
	s_barrier
	s_lshr_b32 s26, s23, 6
	s_mov_b32 s5, 0
	s_add_i32 s27, s27, 0x18000
	v_mov_b32_e32 v15, 0
	v_cmp_neq_f32_e64 s[2:3], 0, v192
	s_andn2_b64 vcc, exec, s[16:17]
	s_mov_b32 s18, 1
	s_cbranch_vccnz .LBB1_86
	s_cmp_eq_u64 s[2:3], 0
	s_cselect_b64 s[2:3], -1, 0
	s_lshl_b32 s4, s26, 2
	s_and_b32 s4, s4, 4
	s_lshl_b32 s19, s25, 14
	s_lshl_b32 s29, s26, 10
	s_cmp_lg_u32 0, -1
	v_bitop3_b32 v0, s4, v200, v208 bitop3:0x36
	s_cselect_b32 s4, 0, 0
	v_lshl_or_b32 v48, s26, 3, v193
	v_mov_b32_e32 v49, 0
	v_or_b32_e32 v4, s19, v1
	s_add_i32 s29, s29, s4
	v_lshlrev_b64 v[2:3], 11, v[48:49]
	s_add_i32 s16, s30, 0x4000
	v_lshlrev_b32_e32 v48, 1, v4
	s_lshl_b32 s4, s24, 6
	s_add_i32 s31, s29, 0xc000
	v_lshl_add_u64 v[4:5], s[14:15], 0, v[48:49]
	s_cmpk_lg_u32 s30, 0x8000
	v_lshl_add_u64 v[2:3], s[6:7], 0, v[2:3]
	v_lshl_add_u64 v[4:5], v[4:5], 0, s[4:5]
	v_lshlrev_b32_e32 v48, 4, v0
	s_cselect_b32 s35, s16, 0
	s_min_u32 s4, s33, 3
	v_lshl_add_u64 v[194:195], v[2:3], 0, v[48:49]
	s_lshl_b32 s4, s4, 18
	v_lshl_add_u64 v[2:3], v[194:195], 0, s[4:5]
	s_add_i32 s4, s29, s30
	s_mov_b32 s6, m0
	s_mov_b32 m0, s4
	s_nop 0
	global_load_lds_dwordx4 v[2:3], off
	s_mov_b32 m0, s6
	s_mov_b64 s[6:7], 0x20000
	v_mov_b32_e32 v191, v49
	v_lshl_add_u64 v[2:3], v[2:3], 0, s[6:7]
	s_addk_i32 s4, 0x2000
	s_mov_b32 s14, m0
	s_mov_b32 m0, s4
	s_nop 0
	global_load_lds_dwordx4 v[2:3], off
	s_mov_b32 m0, s14
	v_lshl_add_u64 v[190:191], v[4:5], 0, v[190:191]
	s_mov_b64 s[14:15], 0x40000
	v_lshl_add_u64 v[2:3], v[190:191], 0, s[14:15]
	s_add_i32 s4, s31, s35
	s_mov_b32 s16, m0
	s_mov_b32 m0, s4
	s_nop 0
	global_load_lds_dwordx4 v[2:3], off
	s_mov_b32 m0, s16
	s_mov_b64 s[16:17], 0x60000
	v_lshl_add_u64 v[2:3], v[190:191], 0, s[16:17]
	v_add_u32_e32 v0, s35, v199
	s_addk_i32 s4, 0x2000
	s_mov_b32 s20, m0
	s_mov_b32 m0, s4
	s_nop 0
	global_load_lds_dwordx4 v[2:3], off
	s_mov_b32 m0, s20
	v_add_u32_e32 v2, v0, v207
	ds_read_b128 v[80:83], v2
	ds_read_b128 v[96:99], v2 offset:4096
	v_add_u32_e32 v2, v0, v206
	ds_read_b128 v[164:167], v2
	ds_read_b128 v[160:163], v2 offset:4096
	v_add_u32_e32 v2, v0, v205
	v_add_u32_e32 v0, v0, v204
	ds_read_b128 v[156:159], v2
	ds_read_b128 v[152:155], v2 offset:4096
	ds_read_b128 v[148:151], v0
	ds_read_b128 v[144:147], v0 offset:4096
	s_add_i32 s4, s35, 0x4000
	s_waitcnt vmcnt(4) lgkmcnt(0)
	s_barrier
	s_cmpk_lg_u32 s35, 0x8000
	s_cselect_b32 s28, s4, 0
	s_cmp_lt_u32 s33, 3
	s_cbranch_scc1 .LBB1_87
	s_lshr_b32 s4, s23, 2
	s_and_b32 s4, s4, 0x3fffffc0
	s_add_u32 s20, s12, s4
	s_addc_u32 s21, s13, 0
	v_lshl_add_u64 v[2:3], s[20:21], 0, v[188:189]
	v_add_lshl_u32 v48, s19, v1, 1
	s_add_u32 s8, s8, s34
	v_lshl_add_u64 v[0:1], v[2:3], 0, v[48:49]
	s_addc_u32 s9, s9, 0
	v_lshl_add_u64 v[0:1], s[8:9], 0, v[0:1]
	s_mov_b64 s[8:9], 0x80000
	v_mov_b32_e32 v48, v49
	v_lshl_add_u64 v[180:181], v[0:1], 0, s[8:9]
	v_mov_b32_e32 v50, v49
	v_mov_b32_e32 v51, v49
	v_mov_b32_e32 v52, v49
	v_mov_b32_e32 v53, v49
	v_mov_b32_e32 v54, v49
	v_mov_b32_e32 v55, v49
	v_mov_b32_e32 v56, v49
	v_mov_b32_e32 v57, v49
	v_mov_b32_e32 v58, v49
	v_mov_b32_e32 v59, v49
	v_mov_b32_e32 v60, v49
	v_mov_b32_e32 v61, v49
	v_mov_b32_e32 v62, v49
	v_mov_b32_e32 v63, v49
	v_mov_b64_e32 v[16:17], v[48:49]
	v_mov_b64_e32 v[0:1], v[48:49]
	v_lshl_add_u32 v182, v202, 2, s27
	v_lshl_add_u32 v183, v203, 2, s27
	s_mov_b32 s36, 5
	s_mov_b32 s34, 0x41000000
	v_mov_b32_e32 v184, 0xff800000
	v_mov_b64_e32 v[18:19], v[50:51]
	v_mov_b64_e32 v[20:21], v[52:53]
	v_mov_b64_e32 v[22:23], v[54:55]
	v_mov_b64_e32 v[24:25], v[56:57]
	v_mov_b64_e32 v[26:27], v[58:59]
	v_mov_b64_e32 v[28:29], v[60:61]
	v_mov_b64_e32 v[30:31], v[62:63]
	v_mov_b64_e32 v[2:3], v[50:51]
	v_mov_b64_e32 v[4:5], v[52:53]
	v_mov_b64_e32 v[6:7], v[54:55]
	v_mov_b64_e32 v[8:9], v[56:57]
	v_mov_b64_e32 v[10:11], v[58:59]
	v_mov_b64_e32 v[12:13], v[60:61]
	v_mov_b64_e32 v[14:15], v[62:63]

.LBB1_135:
	v_mov_b32_e32 v32, 0xff800000
	v_cmp_neq_f32_e32 vcc, 0, v80
	s_nop 1
	v_cndmask_b32_e32 v80, v32, v80, vcc
	v_cmp_neq_f32_e32 vcc, 0, v96
	s_nop 1
	v_cndmask_b32_e32 v96, v32, v96, vcc
	v_cmp_neq_f32_e32 vcc, 0, v81
	s_nop 1
	v_cndmask_b32_e32 v81, v32, v81, vcc
	v_cmp_neq_f32_e32 vcc, 0, v97
	s_nop 1
	v_cndmask_b32_e32 v97, v32, v97, vcc
	v_cmp_neq_f32_e32 vcc, 0, v82
	s_nop 1
	v_cndmask_b32_e32 v82, v32, v82, vcc
	v_cmp_neq_f32_e32 vcc, 0, v98
	s_nop 1
	v_cndmask_b32_e32 v98, v32, v98, vcc
	v_cmp_neq_f32_e32 vcc, 0, v83
	s_nop 1
	v_cndmask_b32_e32 v83, v32, v83, vcc
	v_cmp_neq_f32_e32 vcc, 0, v99
	s_nop 1
	v_cndmask_b32_e32 v99, v32, v99, vcc
	v_cmp_neq_f32_e32 vcc, 0, v84
	s_nop 1
	v_cndmask_b32_e32 v84, v32, v84, vcc
	v_cmp_neq_f32_e32 vcc, 0, v100
	s_nop 1
	v_cndmask_b32_e32 v100, v32, v100, vcc
	v_cmp_neq_f32_e32 vcc, 0, v85
	s_nop 1
	v_cndmask_b32_e32 v85, v32, v85, vcc
	v_cmp_neq_f32_e32 vcc, 0, v101
	s_nop 1
	v_cndmask_b32_e32 v101, v32, v101, vcc
	v_cmp_neq_f32_e32 vcc, 0, v86
	s_nop 1
	v_cndmask_b32_e32 v86, v32, v86, vcc
	v_cmp_neq_f32_e32 vcc, 0, v102
	s_nop 1
	v_cndmask_b32_e32 v102, v32, v102, vcc
	v_cmp_neq_f32_e32 vcc, 0, v87
	s_nop 1
	v_cndmask_b32_e32 v87, v32, v87, vcc
	v_cmp_neq_f32_e32 vcc, 0, v103
	s_nop 1
	v_cndmask_b32_e32 v103, v32, v103, vcc
	v_cmp_neq_f32_e32 vcc, 0, v88
	s_nop 1
	v_cndmask_b32_e32 v88, v32, v88, vcc
	v_cmp_neq_f32_e32 vcc, 0, v104
	s_nop 1
	v_cndmask_b32_e32 v104, v32, v104, vcc
	v_cmp_neq_f32_e32 vcc, 0, v89
	s_nop 1
	v_cndmask_b32_e32 v89, v32, v89, vcc
	v_cmp_neq_f32_e32 vcc, 0, v105
	s_nop 1
	v_cndmask_b32_e32 v105, v32, v105, vcc
	v_cmp_neq_f32_e32 vcc, 0, v90
	s_nop 1
	v_cndmask_b32_e32 v90, v32, v90, vcc
	v_cmp_neq_f32_e32 vcc, 0, v106
	s_nop 1
	v_cndmask_b32_e32 v106, v32, v106, vcc
	v_cmp_neq_f32_e32 vcc, 0, v91
	s_nop 1
	v_cndmask_b32_e32 v91, v32, v91, vcc
	v_cmp_neq_f32_e32 vcc, 0, v107
	s_nop 1
	v_cndmask_b32_e32 v107, v32, v107, vcc
	v_cmp_neq_f32_e32 vcc, 0, v92
	s_nop 1
	v_cndmask_b32_e32 v92, v32, v92, vcc
	v_cmp_neq_f32_e32 vcc, 0, v108
	s_nop 1
	v_cndmask_b32_e32 v108, v32, v108, vcc
	v_cmp_neq_f32_e32 vcc, 0, v93
	s_nop 1
	v_cndmask_b32_e32 v93, v32, v93, vcc
	v_cmp_neq_f32_e32 vcc, 0, v109
	s_nop 1
	v_cndmask_b32_e32 v109, v32, v109, vcc
	v_cmp_neq_f32_e32 vcc, 0, v94
	s_nop 1
	v_cndmask_b32_e32 v94, v32, v94, vcc
	v_cmp_neq_f32_e32 vcc, 0, v110
	s_nop 1
	v_cndmask_b32_e32 v110, v32, v110, vcc
	v_cmp_neq_f32_e32 vcc, 0, v95
	s_nop 1
	v_cndmask_b32_e32 v95, v32, v95, vcc
	v_cmp_neq_f32_e32 vcc, 0, v111
	s_nop 1
	v_cndmask_b32_e32 v111, v32, v111, vcc
	s_branch .LBB1_93
	s_nop 0
	s_nop 0
	s_nop 0
	s_nop 0
	s_nop 0
	s_nop 0
	s_nop 0
	s_nop 0
	s_nop 0
	s_nop 0
	s_nop 0
	s_nop 0
	s_nop 0
	s_nop 0
	s_nop 0
	s_nop 0
	s_nop 0
	s_nop 0
	s_nop 0
	s_nop 0
	s_nop 0
	s_nop 0
	s_nop 0
	s_nop 0
	s_nop 0
	s_nop 0
	s_nop 0
	s_nop 0
	s_nop 0
	s_nop 0
	s_nop 0
	s_endpgm
